# pointwise-conv GEMM epilogue: 16-B stores lane-transposed through ds_bpermute (coalesced 64-B per lane quad)
# speedup vs baseline: 1.0060x; 1.0060x over previous
; #define PG8_ST16(rs, b0, p, v) __builtin_amdgcn_raw_buffer_store_b128(v, rs, (int)((const char*)(p) - (const char*)(b0)), 0, 16)
; __device__ __forceinline__ unsigned cvt_pk_bf16(float lo, float hi) { unsigned r; asm volatile("v_cvt_pk_bf16_f32 %0, %1, %2" : "=v"(r) : "v"(lo), "v"(hi)); return r; }
;     __device__ __forceinline__ void operator()(const f32x4 (&acc)[2][2][4][2], const Unit& u, int wr, int wc, int fr, int fq) const {
;     ...
;         for (int ai = 0; ai < 2; ++ai)
; #pragma unroll
;             for (int m = 0; m < 4; ++m) { bf16_t* rowp = base + (size_t)(row0 + ai * HALF + m * 16) * ldc + col0;
; #pragma unroll
;                 for (int bj = 0; bj < 2; ++bj) { f32x4 v0 = acc[ai][bj][m][0] + bv[bj][0], v1 = acc[ai][bj][m][1] + bv[bj][1];
;                     if (ACT == 1) { f32x2 a = gelu_pk((f32x2){v0[0], v0[1]}), b = gelu_pk((f32x2){v0[2], v0[3]}), c = gelu_pk((f32x2){v1[0], v1[1]}), d = gelu_pk((f32x2){v1[2], v1[3]});
;                         v0 = (f32x4){a.x, a.y, b.x, b.y}; v1 = (f32x4){c.x, c.y, d.x, d.y}; }
;                     v0 = v0 * sc; v1 = v1 * sc; u32x4 w; w.x = cvt_pk_bf16(v0[0], v0[1]); w.y = cvt_pk_bf16(v0[2], v0[3]); w.z = cvt_pk_bf16(v1[0], v1[1]); w.w = cvt_pk_bf16(v1[2], v1[3]);
;                     PG8_ST16(rs_, base, rowp + bj * HALF, w); } }
.LBB0_661:
	v_lshl_add_u32 v28, s35, 8, v3
	v_lshl_or_b32 v20, s43, 8, v151
	v_ashrrev_i32_e32 v21, 31, v20
	v_ashrrev_i32_e32 v29, 31, v28
	v_lshl_add_u64 v[30:31], v[20:21], 1, s[10:11]
	v_lshrrev_b32_e32 v252, 2, v215
	v_and_b32_e32 v246, 15, v215
	v_sub_u32_e32 v252, v252, v246
	v_and_b32_e32 v246, 3, v215
	v_lshrrev_b32_e32 v247, 4, v215
	v_sub_u32_e32 v247, v246, v247
	v_lshlrev_b32_e32 v248, 10, v252
	v_lshl_add_u32 v248, v247, 4, v248
	v_ashrrev_i32_e32 v249, 31, v248
	v_lshl_add_u64 v[30:31], v[30:31], 0, v[248:249]
	v_and_b32_e32 v252, 60, v215
	v_lshl_or_b32 v252, v246, 6, v252
	v_lshlrev_b64 v[20:21], 10, v[28:29]
	v_lshl_add_u64 v[154:155], v[30:31], 0, v[20:21]
	v_cvt_pk_bf16_f32 v20, v128, v129
	v_cvt_pk_bf16_f32 v21, v130, v131
	v_cvt_pk_bf16_f32 v22, v124, v125
	v_cvt_pk_bf16_f32 v23, v126, v127
	v_mov_b64_e32 v[242:243], v[154:155]
	ds_bpermute_b32 v234, v252, v20
	ds_bpermute_b32 v235, v252, v21
	ds_bpermute_b32 v236, v252, v22
	ds_bpermute_b32 v237, v252, v23
	v_readlane_b32 s44, v254, 3
	v_readlane_b32 s47, v254, 6
	v_cvt_pk_bf16_f32 v20, v144, v145
	v_cvt_pk_bf16_f32 v21, v142, v143
	v_cvt_pk_bf16_f32 v22, v148, v149
	v_cvt_pk_bf16_f32 v23, v146, v147
	v_mov_b64_e32 v[244:245], v[154:155]
	ds_bpermute_b32 v238, v252, v20
	ds_bpermute_b32 v239, v252, v21
	ds_bpermute_b32 v240, v252, v22
	ds_bpermute_b32 v241, v252, v23
	s_waitcnt lgkmcnt(4)
	global_store_dwordx4 v[242:243], v[234:237], off
	s_mov_b64 s[18:19], 0x20000
	v_readlane_b32 s45, v254, 4
	v_or_b32_e32 v20, 16, v28
	v_ashrrev_i32_e32 v21, 31, v20
	v_lshlrev_b64 v[20:21], 10, v[20:21]
	v_lshl_add_u64 v[124:125], v[30:31], 0, v[20:21]
	v_cvt_pk_bf16_f32 v20, v106, v107
	v_cvt_pk_bf16_f32 v21, v104, v105
	v_cvt_pk_bf16_f32 v22, v114, v115
	v_cvt_pk_bf16_f32 v23, v112, v113
	v_mov_b64_e32 v[242:243], v[124:125]
	ds_bpermute_b32 v234, v252, v20
	ds_bpermute_b32 v235, v252, v21
	ds_bpermute_b32 v236, v252, v22
	ds_bpermute_b32 v237, v252, v23
	s_waitcnt lgkmcnt(4)
	global_store_dwordx4 v[244:245], v[238:241], off offset:256
	v_readlane_b32 s46, v254, 5
	s_nop 0
	v_cvt_pk_bf16_f32 v20, v118, v119
	v_cvt_pk_bf16_f32 v21, v116, v117
	v_cvt_pk_bf16_f32 v22, v122, v123
	v_cvt_pk_bf16_f32 v23, v120, v121
	v_mov_b64_e32 v[244:245], v[124:125]
	ds_bpermute_b32 v238, v252, v20
	ds_bpermute_b32 v239, v252, v21
	ds_bpermute_b32 v240, v252, v22
	ds_bpermute_b32 v241, v252, v23
	s_waitcnt lgkmcnt(4)
	global_store_dwordx4 v[242:243], v[234:237], off
	s_nop 1
	v_or_b32_e32 v20, 32, v28
	v_ashrrev_i32_e32 v21, 31, v20
	v_lshlrev_b64 v[20:21], 10, v[20:21]
	v_lshl_add_u64 v[104:105], v[30:31], 0, v[20:21]
	v_cvt_pk_bf16_f32 v20, v90, v91
	v_cvt_pk_bf16_f32 v21, v88, v89
	v_cvt_pk_bf16_f32 v22, v98, v99
	v_cvt_pk_bf16_f32 v23, v96, v97
	v_mov_b64_e32 v[242:243], v[104:105]
	ds_bpermute_b32 v234, v252, v20
	ds_bpermute_b32 v235, v252, v21
	ds_bpermute_b32 v236, v252, v22
	ds_bpermute_b32 v237, v252, v23
	s_waitcnt lgkmcnt(4)
	global_store_dwordx4 v[244:245], v[238:241], off offset:256
	s_nop 1
	v_cvt_pk_bf16_f32 v20, v102, v103
	v_cvt_pk_bf16_f32 v21, v100, v101
	v_cvt_pk_bf16_f32 v22, v110, v111
	v_cvt_pk_bf16_f32 v23, v108, v109
	v_mov_b64_e32 v[244:245], v[104:105]
	ds_bpermute_b32 v238, v252, v20
	ds_bpermute_b32 v239, v252, v21
	ds_bpermute_b32 v240, v252, v22
	ds_bpermute_b32 v241, v252, v23
	s_waitcnt lgkmcnt(4)
	global_store_dwordx4 v[242:243], v[234:237], off
	s_nop 1
	v_or_b32_e32 v20, 48, v28
	v_ashrrev_i32_e32 v21, 31, v20
	v_lshlrev_b64 v[20:21], 10, v[20:21]
	v_lshl_add_u64 v[28:29], v[30:31], 0, v[20:21]
	v_cvt_pk_bf16_f32 v20, v78, v79
	v_cvt_pk_bf16_f32 v21, v76, v77
	v_cvt_pk_bf16_f32 v22, v82, v83
	v_cvt_pk_bf16_f32 v23, v80, v81
	v_mov_b64_e32 v[242:243], v[28:29]
	ds_bpermute_b32 v234, v252, v20
	ds_bpermute_b32 v235, v252, v21
	ds_bpermute_b32 v236, v252, v22
	ds_bpermute_b32 v237, v252, v23
	s_waitcnt lgkmcnt(4)
	global_store_dwordx4 v[244:245], v[238:241], off offset:256
	v_add_co_u32_e32 v30, vcc, s47, v154
	s_nop 0
	v_cvt_pk_bf16_f32 v20, v72, v73
	v_cvt_pk_bf16_f32 v21, v74, v75
	v_cvt_pk_bf16_f32 v22, v68, v69
	v_cvt_pk_bf16_f32 v23, v70, v71
	v_mov_b64_e32 v[244:245], v[28:29]
	ds_bpermute_b32 v238, v252, v20
	ds_bpermute_b32 v239, v252, v21
	ds_bpermute_b32 v240, v252, v22
	ds_bpermute_b32 v241, v252, v23
	s_waitcnt lgkmcnt(4)
; #define PG8_ST16(rs, b0, p, v) __builtin_amdgcn_raw_buffer_store_b128(v, rs, (int)((const char*)(p) - (const char*)(b0)), 0, 16)
; __device__ __forceinline__ unsigned cvt_pk_bf16(float lo, float hi) { unsigned r; asm volatile("v_cvt_pk_bf16_f32 %0, %1, %2" : "=v"(r) : "v"(lo), "v"(hi)); return r; }
;     __device__ __forceinline__ void operator()(const f32x4 (&acc)[2][2][4][2], const Unit& u, int wr, int wc, int fr, int fq) const {
;     ...
;             for (int m = 0; m < 4; ++m) { bf16_t* rowp = base + (size_t)(row0 + ai * HALF + m * 16) * ldc + col0;
; #pragma unroll
;                 for (int bj = 0; bj < 2; ++bj) { f32x4 v0 = acc[ai][bj][m][0] + bv[bj][0], v1 = acc[ai][bj][m][1] + bv[bj][1];
;                     if (ACT == 1) { f32x2 a = gelu_pk((f32x2){v0[0], v0[1]}), b = gelu_pk((f32x2){v0[2], v0[3]}), c = gelu_pk((f32x2){v1[0], v1[1]}), d = gelu_pk((f32x2){v1[2], v1[3]});
;                         v0 = (f32x4){a.x, a.y, b.x, b.y}; v1 = (f32x4){c.x, c.y, d.x, d.y}; }
;                     v0 = v0 * sc; v1 = v1 * sc; u32x4 w; w.x = cvt_pk_bf16(v0[0], v0[1]); w.y = cvt_pk_bf16(v0[2], v0[3]); w.z = cvt_pk_bf16(v1[0], v1[1]); w.w = cvt_pk_bf16(v1[2], v1[3]);
;                     PG8_ST16(rs_, base, rowp + bj * HALF, w); } }
	global_store_dwordx4 v[242:243], v[234:237], off
	v_lshl_add_u64 v[28:29], v[154:155], 0, s[18:19]
	v_addc_co_u32_e32 v31, vcc, 0, v155, vcc
	v_cvt_pk_bf16_f32 v20, v64, v65
	v_cvt_pk_bf16_f32 v21, v66, v67
	v_cvt_pk_bf16_f32 v22, v60, v61
	v_cvt_pk_bf16_f32 v23, v62, v63
	s_mov_b64 s[18:19], 0x24000
	v_mov_b64_e32 v[242:243], v[30:31]
	ds_bpermute_b32 v234, v252, v20
	ds_bpermute_b32 v235, v252, v21
	ds_bpermute_b32 v236, v252, v22
	ds_bpermute_b32 v237, v252, v23
	s_waitcnt lgkmcnt(4)
	global_store_dwordx4 v[244:245], v[238:241], off offset:256
	s_nop 1
	v_cvt_pk_bf16_f32 v20, v86, v87
	v_cvt_pk_bf16_f32 v21, v84, v85
	v_cvt_pk_bf16_f32 v22, v94, v95
	v_cvt_pk_bf16_f32 v23, v92, v93
	v_mov_b64_e32 v[244:245], v[28:29]
	ds_bpermute_b32 v238, v252, v20
	ds_bpermute_b32 v239, v252, v21
	ds_bpermute_b32 v240, v252, v22
	ds_bpermute_b32 v241, v252, v23
	s_waitcnt lgkmcnt(4)
	global_store_dwordx4 v[242:243], v[234:237], off
	v_lshl_add_u64 v[28:29], v[154:155], 0, s[18:19]
	s_mov_b32 s18, 0x24000
	v_add_co_u32_e32 v30, vcc, s18, v154
	v_cvt_pk_bf16_f32 v20, v42, v43
	v_cvt_pk_bf16_f32 v21, v40, v41
	v_cvt_pk_bf16_f32 v22, v50, v51
	v_cvt_pk_bf16_f32 v23, v48, v49
	s_nop 1
	v_addc_co_u32_e32 v31, vcc, 0, v155, vcc
	s_mov_b64 s[18:19], 0x28000
	v_mov_b64_e32 v[242:243], v[30:31]
	ds_bpermute_b32 v234, v252, v20
	ds_bpermute_b32 v235, v252, v21
	ds_bpermute_b32 v236, v252, v22
	ds_bpermute_b32 v237, v252, v23
	s_waitcnt lgkmcnt(4)
	global_store_dwordx4 v[244:245], v[238:241], off offset:256
	s_nop 1
	v_cvt_pk_bf16_f32 v20, v54, v55
	v_cvt_pk_bf16_f32 v21, v52, v53
	v_cvt_pk_bf16_f32 v22, v58, v59
	v_cvt_pk_bf16_f32 v23, v56, v57
	v_mov_b64_e32 v[244:245], v[28:29]
	ds_bpermute_b32 v238, v252, v20
	ds_bpermute_b32 v239, v252, v21
	ds_bpermute_b32 v240, v252, v22
	ds_bpermute_b32 v241, v252, v23
	s_waitcnt lgkmcnt(4)
	global_store_dwordx4 v[242:243], v[234:237], off
	v_lshl_add_u64 v[28:29], v[154:155], 0, s[18:19]
	s_mov_b32 s18, 0x28000
	v_cvt_pk_bf16_f32 v20, v26, v27
	v_cvt_pk_bf16_f32 v21, v24, v25
	v_add_co_u32_e32 v24, vcc, s18, v154
	v_cvt_pk_bf16_f32 v22, v34, v35
	v_cvt_pk_bf16_f32 v23, v32, v33
	s_mov_b64 s[18:19], 0x2c000
	s_nop 0
	v_addc_co_u32_e32 v25, vcc, 0, v155, vcc
	v_mov_b64_e32 v[242:243], v[24:25]
	ds_bpermute_b32 v234, v252, v20
	ds_bpermute_b32 v235, v252, v21
	ds_bpermute_b32 v236, v252, v22
	ds_bpermute_b32 v237, v252, v23
	s_waitcnt lgkmcnt(4)
	global_store_dwordx4 v[244:245], v[238:241], off offset:256
	v_lshl_add_u64 v[24:25], v[154:155], 0, s[18:19]
	s_nop 0
	v_cvt_pk_bf16_f32 v20, v38, v39
	v_cvt_pk_bf16_f32 v21, v36, v37
	v_cvt_pk_bf16_f32 v22, v46, v47
	v_cvt_pk_bf16_f32 v23, v44, v45
	v_mov_b64_e32 v[244:245], v[28:29]
	ds_bpermute_b32 v238, v252, v20
	ds_bpermute_b32 v239, v252, v21
	ds_bpermute_b32 v240, v252, v22
	ds_bpermute_b32 v241, v252, v23
	s_waitcnt lgkmcnt(4)
	global_store_dwordx4 v[242:243], v[234:237], off
	s_nop 1
	v_cvt_pk_bf16_f32 v20, v14, v15
	v_cvt_pk_bf16_f32 v21, v12, v13
	v_add_co_u32_e32 v12, vcc, 0x2c000, v154
	v_cvt_pk_bf16_f32 v22, v18, v19
	v_cvt_pk_bf16_f32 v23, v16, v17
	s_nop 1
	v_addc_co_u32_e32 v13, vcc, 0, v155, vcc
	s_and_b64 vcc, exec, s[2:3]
	s_mov_b64 s[2:3], -1
	v_mov_b64_e32 v[242:243], v[12:13]
	ds_bpermute_b32 v234, v252, v20
	ds_bpermute_b32 v235, v252, v21
	ds_bpermute_b32 v236, v252, v22
	ds_bpermute_b32 v237, v252, v23
	s_waitcnt lgkmcnt(4)
	global_store_dwordx4 v[244:245], v[238:241], off offset:256
	v_cvt_pk_bf16_f32 v8, v8, v9
	v_cvt_pk_bf16_f32 v9, v10, v11
	v_cvt_pk_bf16_f32 v10, v4, v5
	v_cvt_pk_bf16_f32 v11, v6, v7
	v_mov_b64_e32 v[244:245], v[24:25]
	ds_bpermute_b32 v238, v252, v8
	ds_bpermute_b32 v239, v252, v9
	ds_bpermute_b32 v240, v252, v10
	ds_bpermute_b32 v241, v252, v11
	s_waitcnt lgkmcnt(4)
	global_store_dwordx4 v[242:243], v[234:237], off
	s_waitcnt lgkmcnt(0)
	global_store_dwordx4 v[244:245], v[238:241], off offset:256
	s_cbranch_vccnz .LBB0_644
	s_andn2_b64 vcc, exec, s[8:9]
	s_cbranch_vccnz .LBB0_643
	s_barrier
	s_branch .LBB0_643
